# v60 + P1 lag-kernel loop: per-lane line prefetch of the PW / BBAR / cre / cim lines before the 16 dependent trips
# baseline (speedup 1.0000x reference)
; #define AIN(i) ((const float*)ldp(lds, (i)))
; __device__ __forceinline__ void ph1(LAS unsigned char* lds, int tid, int G, int bid) {
;     ...
;       for (int i = gt; i < SG * 2 * LC * 64; i += NGT) { const int hq = i & 3, ho = (i >> 2) & 15, k = (i >> 6) & 31, gd = i >> 11, g = gd >> 1, dir = gd & 1;
;           const float* cre = AIN(ICRE) + ((size_t)(dir * SG + g) * SH + ho) * SP; const float* cim = AIN(ICIM) + ((size_t)(dir * SG + g) * SH + ho) * SP;
;           f32x4 s = (f32x4){0.f, 0.f, 0.f, 0.f};
; #pragma unroll 4
;           for (int p = 0; p < SP; ++p) { const f32x2 pw = PW[((size_t)gd * SP + p) * 33 + k]; const f32x4* bq = (const f32x4*)(BBAR + ((size_t)gd * SP + p) * SH + 4 * hq); const f32x4 b01 = bq[0], b23 = bq[1]; const float cr = cre[p], ci = cim[p];
;               const float tr = cr * pw.x - ci * pw.y, ti = cr * pw.y + ci * pw.x;
;               s.x += tr * b01.x - ti * b01.y; s.y += tr * b01.z - ti * b01.w; s.z += tr * b23.x - ti * b23.y; s.w += tr * b23.z - ti * b23.w; }
.LBB0_198:
	ds_read_b32 v2, v7
	ds_read_b32 v3, v11
	v_ashrrev_i32_e32 v14, 11, v26
	ds_read_b32 v16, v24
	ds_read_b32 v17, v25
	v_ashrrev_i32_e32 v15, 12, v26
	s_waitcnt lgkmcnt(0)
	v_readfirstlane_b32 s18, v2
	v_lshlrev_b32_e32 v2, 5, v14
	v_and_b32_e32 v2, 32, v2
	v_add_u32_e32 v2, v2, v15
	v_readfirstlane_b32 s19, v3
	v_ashrrev_i32_e32 v3, 31, v2
	v_lshlrev_b32_e32 v5, 6, v26
	v_ashrrev_i32_e32 v15, 31, v14
	v_lshlrev_b64 v[2:3], 12, v[2:3]
	v_lshrrev_b32_e32 v4, 3, v26
	v_readfirstlane_b32 s22, v16
	v_readfirstlane_b32 s23, v17
	v_lshlrev_b64 v[16:17], 13, v[14:15]
	v_mul_i32_i24_e32 v18, 0x4200, v14
	v_and_or_b32 v2, v5, s20, v2
	v_lshrrev_b32_e32 v8, 6, v26
	v_lshrrev_b32_e32 v13, 2, v26
	v_or_b32_e32 v16, v10, v16
	v_mul_hi_i32_i24_e32 v19, 0x4200, v14
	v_and_or_b32 v18, v4, s5, v18
	v_lshl_add_u64 v[20:21], s[22:23], 0, v[2:3]
	v_lshl_add_u64 v[22:23], s[18:19], 0, v[2:3]
	s_mov_b64 s[18:19], 0
	v_mov_b32_e32 v2, 0
	v_mov_b32_e32 v3, v9
	v_mov_b32_e32 v4, 0
	v_mov_b32_e32 v5, v9
	v_and_b32_e32 v82, 63, v0
	v_mul_u32_u24_e32 v74, 0x108, v82
	v_mov_b32_e32 v75, 0
	v_lshlrev_b32_e32 v76, 7, v82
	v_mov_b32_e32 v77, 0
	v_lshl_add_u64 v[32:33], s[6:7], 0, v[18:19]
	v_add_co_u32_e32 v32, vcc, 0x600000, v32
	s_nop 1
	v_addc_co_u32_e32 v33, vcc, 0, v33, vcc
	v_lshl_add_u64 v[32:33], v[32:33], 0, v[74:75]
	flat_load_dword v78, v[32:33]
	v_lshl_add_u64 v[40:41], s[6:7], 0, v[16:17]
	v_add_co_u32_e32 v40, vcc, 0x800000, v40
	s_nop 1
	v_addc_co_u32_e32 v41, vcc, 0, v41, vcc
	v_lshl_add_u64 v[40:41], v[40:41], 0, v[76:77]
	flat_load_dword v79, v[40:41]
	flat_load_dword v80, v[22:23] offset:128
	flat_load_dword v81, v[20:21] offset:128
